# speedup vs baseline: 1.0055x; 1.0055x over previous
.Lg1_noX:
	v_permlane16_swap_b32_e32 v158, v160
	v_permlane16_swap_b32_e32 v159, v161
	global_store_dwordx4 v228, v[158:161], s[58:59] offset:128 nt
	v_exp_f32_e32 v130, v90
	v_exp_f32_e32 v131, v91
	v_exp_f32_e32 v132, v92
	v_exp_f32_e32 v133, v93
	v_exp_f32_e32 v142, v42
	v_exp_f32_e32 v143, v43
	v_exp_f32_e32 v144, v44
	v_exp_f32_e32 v145, v45
	v_exp_f32_e32 v176, v126
	v_exp_f32_e32 v177, v127
	v_exp_f32_e32 v178, v128
	v_exp_f32_e32 v179, v129
	v_exp_f32_e32 v232, v58
	v_exp_f32_e32 v233, v59
	v_exp_f32_e32 v234, v60
	v_exp_f32_e32 v235, v61
	v_pk_fma_f32 v[130:131], v[130:131], -0.5, -0.5 op_sel_hi:[1,0,0]
	v_pk_fma_f32 v[132:133], v[132:133], -0.5, -0.5 op_sel_hi:[1,0,0]
	v_pk_fma_f32 v[142:143], v[142:143], -0.5, -0.5 op_sel_hi:[1,0,0]
	v_pk_fma_f32 v[144:145], v[144:145], -0.5, -0.5 op_sel_hi:[1,0,0]
	v_pk_fma_f32 v[176:177], v[176:177], -0.5, -0.5 op_sel_hi:[1,0,0]
	v_pk_fma_f32 v[178:179], v[178:179], -0.5, -0.5 op_sel_hi:[1,0,0]
	v_pk_fma_f32 v[232:233], v[232:233], -0.5, -0.5 op_sel_hi:[1,0,0]
	v_pk_fma_f32 v[234:235], v[234:235], -0.5, -0.5 op_sel_hi:[1,0,0]
	v_pk_mul_f32 v[134:135], v[130:131], v[132:133]
	v_pk_mul_f32 v[146:147], v[142:143], v[144:145]
	v_pk_mul_f32 v[180:181], v[176:177], v[178:179]
	v_pk_mul_f32 v[236:237], v[232:233], v[234:235]
	v_mul_f32_e32 v188, v134, v135
	v_mul_f32_e32 v190, v146, v147
	v_mul_f32_e32 v189, v180, v181
	v_mul_f32_e32 v191, v236, v237
	v_pk_mul_f32 v[192:193], v[188:189], v[190:191]
	v_mul_f32_e32 v174, v192, v193
	v_rcp_f32_e32 v173, v174
	v_pk_add_f32 v[164:165], v[164:165], v[90:91]
	v_pk_add_f32 v[164:165], v[164:165], v[92:93]
	v_pk_add_f32 v[164:165], v[164:165], v[42:43]
	v_pk_add_f32 v[164:165], v[164:165], v[44:45]
	v_pk_add_f32 v[164:165], v[164:165], v[126:127]
	v_pk_add_f32 v[164:165], v[164:165], v[128:129]
	v_pk_add_f32 v[164:165], v[164:165], v[58:59]
	v_pk_add_f32 v[164:165], v[164:165], v[60:61]
	v_pk_mul_f32 v[230:231], v[172:173], v[192:193] op_sel:[1,1] op_sel_hi:[1,0]
	v_pk_mul_f32 v[192:193], v[230:231], v[190:191]
	v_pk_mul_f32 v[190:191], v[230:231], v[188:189]
	v_pk_mul_f32 v[136:137], v[192:193], v[134:135] op_sel:[0,1] op_sel_hi:[0,0]
	v_pk_mul_f32 v[148:149], v[190:191], v[146:147] op_sel:[0,1] op_sel_hi:[0,0]
	v_pk_mul_f32 v[182:183], v[192:193], v[180:181] op_sel:[1,1] op_sel_hi:[1,0]
	v_pk_mul_f32 v[238:239], v[190:191], v[236:237] op_sel:[1,1] op_sel_hi:[1,0]
	v_pk_fma_f32 v[138:139], v[136:137], v[132:133], 1.0 op_sel_hi:[1,1,0]
	v_pk_fma_f32 v[140:141], v[136:137], v[130:131], 1.0 op_sel_hi:[1,1,0]
	v_pk_fma_f32 v[150:151], v[148:149], v[144:145], 1.0 op_sel_hi:[1,1,0]
	v_pk_fma_f32 v[152:153], v[148:149], v[142:143], 1.0 op_sel_hi:[1,1,0]
	v_pk_fma_f32 v[184:185], v[182:183], v[178:179], 1.0 op_sel_hi:[1,1,0]
	v_pk_fma_f32 v[186:187], v[182:183], v[176:177], 1.0 op_sel_hi:[1,1,0]
	v_pk_fma_f32 v[240:241], v[238:239], v[234:235], 1.0 op_sel_hi:[1,1,0]
	v_pk_fma_f32 v[242:243], v[238:239], v[232:233], 1.0 op_sel_hi:[1,1,0]
	v_cvt_pk_bf16_f32 v154, v138, v139
	v_cvt_pk_bf16_f32 v155, v140, v141
	v_cvt_pk_bf16_f32 v156, v150, v151
	v_cvt_pk_bf16_f32 v157, v152, v153
	v_cvt_pk_bf16_f32 v158, v184, v185
	v_cvt_pk_bf16_f32 v159, v186, v187
	v_cvt_pk_bf16_f32 v160, v240, v241
	v_cvt_pk_bf16_f32 v161, v242, v243
	ds_read_b128 v[90:93], v172 offset:512
	ds_read_b128 v[42:45], v172 offset:576
	ds_read_b128 v[126:129], v172 offset:640
	ds_read_b128 v[58:61], v172 offset:704
	v_permlane16_swap_b32_e32 v154, v156
	v_permlane16_swap_b32_e32 v155, v157
	global_store_dwordx4 v228, v[154:157], s[62:63] nt
	v_permlane16_swap_b32_e32 v158, v160
	v_permlane16_swap_b32_e32 v159, v161
	global_store_dwordx4 v228, v[158:161], s[62:63] offset:128 nt
	v_log_f32_e32 v166, v162
	v_log_f32_e32 v170, v174
	v_add_f32_e32 v168, v164, v165
	v_mul_f32_e32 v168, 0xbeb17218, v168
	v_add_f32_e32 v166, v166, v170
	v_fmac_f32_e32 v168, 0x3f317218, v166
	v_mov_b32_e32 v169, v168
	s_nop 1
	v_permlane16_swap_b32_e32 v168, v169
	v_add_f32_e32 v168, v168, v169
	v_mov_b32_e32 v169, v168
	s_nop 1
	v_permlane32_swap_b32_e32 v168, v169
	v_add_f32_e32 v168, v168, v169
	s_mov_b64 exec, s[0:1]
	global_store_dword v229, v168, s[66:67]
	s_mov_b64 exec, -1
	v_exp_f32_e32 v130, v110
	v_exp_f32_e32 v131, v111
	v_exp_f32_e32 v132, v112
	v_exp_f32_e32 v133, v113
	v_exp_f32_e32 v142, v74
	v_exp_f32_e32 v143, v75
	v_exp_f32_e32 v144, v76
	v_exp_f32_e32 v145, v77
	v_exp_f32_e32 v176, v102
	v_exp_f32_e32 v177, v103
	v_exp_f32_e32 v178, v104
	v_exp_f32_e32 v179, v105
	v_exp_f32_e32 v232, v66
	v_exp_f32_e32 v233, v67
	v_exp_f32_e32 v234, v68
	v_exp_f32_e32 v235, v69
	v_pk_fma_f32 v[130:131], v[130:131], -0.5, -0.5 op_sel_hi:[1,0,0]
	v_pk_fma_f32 v[132:133], v[132:133], -0.5, -0.5 op_sel_hi:[1,0,0]
	v_pk_fma_f32 v[142:143], v[142:143], -0.5, -0.5 op_sel_hi:[1,0,0]
	v_pk_fma_f32 v[144:145], v[144:145], -0.5, -0.5 op_sel_hi:[1,0,0]
	v_pk_fma_f32 v[176:177], v[176:177], -0.5, -0.5 op_sel_hi:[1,0,0]
	v_pk_fma_f32 v[178:179], v[178:179], -0.5, -0.5 op_sel_hi:[1,0,0]
	v_pk_fma_f32 v[232:233], v[232:233], -0.5, -0.5 op_sel_hi:[1,0,0]
	v_pk_fma_f32 v[234:235], v[234:235], -0.5, -0.5 op_sel_hi:[1,0,0]
	v_pk_mul_f32 v[134:135], v[130:131], v[132:133]
	v_pk_mul_f32 v[146:147], v[142:143], v[144:145]
	v_pk_mul_f32 v[180:181], v[176:177], v[178:179]
	v_pk_mul_f32 v[236:237], v[232:233], v[234:235]
	v_mul_f32_e32 v188, v134, v135
	v_mul_f32_e32 v190, v146, v147
	v_mul_f32_e32 v189, v180, v181
	v_mul_f32_e32 v191, v236, v237
	v_pk_mul_f32 v[192:193], v[188:189], v[190:191]
	v_mul_f32_e32 v162, v192, v193
	v_rcp_f32_e32 v173, v162
	v_pk_add_f32 v[164:165], v[110:111], v[112:113]
	v_pk_add_f32 v[164:165], v[164:165], v[74:75]
	v_pk_add_f32 v[164:165], v[164:165], v[76:77]
	v_pk_add_f32 v[164:165], v[164:165], v[102:103]
	v_pk_add_f32 v[164:165], v[164:165], v[104:105]
	v_pk_add_f32 v[164:165], v[164:165], v[66:67]
	v_pk_add_f32 v[164:165], v[164:165], v[68:69]
	v_pk_mul_f32 v[230:231], v[172:173], v[192:193] op_sel:[1,1] op_sel_hi:[1,0]
	v_pk_mul_f32 v[192:193], v[230:231], v[190:191]
	v_pk_mul_f32 v[190:191], v[230:231], v[188:189]
	v_pk_mul_f32 v[136:137], v[192:193], v[134:135] op_sel:[0,1] op_sel_hi:[0,0]
	v_pk_mul_f32 v[148:149], v[190:191], v[146:147] op_sel:[0,1] op_sel_hi:[0,0]
	v_pk_mul_f32 v[182:183], v[192:193], v[180:181] op_sel:[1,1] op_sel_hi:[1,0]
	v_pk_mul_f32 v[238:239], v[190:191], v[236:237] op_sel:[1,1] op_sel_hi:[1,0]
	v_pk_fma_f32 v[138:139], v[136:137], v[132:133], 1.0 op_sel_hi:[1,1,0]
	v_pk_fma_f32 v[140:141], v[136:137], v[130:131], 1.0 op_sel_hi:[1,1,0]
	v_pk_fma_f32 v[150:151], v[148:149], v[144:145], 1.0 op_sel_hi:[1,1,0]
	v_pk_fma_f32 v[152:153], v[148:149], v[142:143], 1.0 op_sel_hi:[1,1,0]
	v_pk_fma_f32 v[184:185], v[182:183], v[178:179], 1.0 op_sel_hi:[1,1,0]
	v_pk_fma_f32 v[186:187], v[182:183], v[176:177], 1.0 op_sel_hi:[1,1,0]
	v_pk_fma_f32 v[240:241], v[238:239], v[234:235], 1.0 op_sel_hi:[1,1,0]
	v_pk_fma_f32 v[242:243], v[238:239], v[232:233], 1.0 op_sel_hi:[1,1,0]
	v_cvt_pk_bf16_f32 v154, v138, v139
	v_cvt_pk_bf16_f32 v155, v140, v141
	v_cvt_pk_bf16_f32 v156, v150, v151
	v_cvt_pk_bf16_f32 v157, v152, v153
	v_cvt_pk_bf16_f32 v158, v184, v185
	v_cvt_pk_bf16_f32 v159, v186, v187
	v_cvt_pk_bf16_f32 v160, v240, v241
	v_cvt_pk_bf16_f32 v161, v242, v243
	ds_read_b128 v[110:113], v172
	ds_read_b128 v[74:77], v172 offset:64
	ds_read_b128 v[102:105], v172 offset:128
	ds_read_b128 v[66:69], v172 offset:192
	v_permlane16_swap_b32_e32 v154, v156
	v_permlane16_swap_b32_e32 v155, v157
	global_store_dwordx4 v228, v[154:157], s[58:59] offset:2048 nt
	v_permlane16_swap_b32_e32 v158, v160
	v_permlane16_swap_b32_e32 v159, v161
	global_store_dwordx4 v228, v[158:161], s[58:59] offset:2176 nt
	v_exp_f32_e32 v130, v86
	v_exp_f32_e32 v131, v87
	v_exp_f32_e32 v132, v88
	v_exp_f32_e32 v133, v89
	v_exp_f32_e32 v142, v38
	v_exp_f32_e32 v143, v39
	v_exp_f32_e32 v144, v40
	v_exp_f32_e32 v145, v41
	v_exp_f32_e32 v176, v122
	v_exp_f32_e32 v177, v123
	v_exp_f32_e32 v178, v124
	v_exp_f32_e32 v179, v125
	v_exp_f32_e32 v232, v50
	v_exp_f32_e32 v233, v51
	v_exp_f32_e32 v234, v52
	v_exp_f32_e32 v235, v53
	v_pk_fma_f32 v[130:131], v[130:131], -0.5, -0.5 op_sel_hi:[1,0,0]
	v_pk_fma_f32 v[132:133], v[132:133], -0.5, -0.5 op_sel_hi:[1,0,0]
	v_pk_fma_f32 v[142:143], v[142:143], -0.5, -0.5 op_sel_hi:[1,0,0]
	v_pk_fma_f32 v[144:145], v[144:145], -0.5, -0.5 op_sel_hi:[1,0,0]
	v_pk_fma_f32 v[176:177], v[176:177], -0.5, -0.5 op_sel_hi:[1,0,0]
	v_pk_fma_f32 v[178:179], v[178:179], -0.5, -0.5 op_sel_hi:[1,0,0]
	v_pk_fma_f32 v[232:233], v[232:233], -0.5, -0.5 op_sel_hi:[1,0,0]
	v_pk_fma_f32 v[234:235], v[234:235], -0.5, -0.5 op_sel_hi:[1,0,0]
	v_pk_mul_f32 v[134:135], v[130:131], v[132:133]
	v_pk_mul_f32 v[146:147], v[142:143], v[144:145]
	v_pk_mul_f32 v[180:181], v[176:177], v[178:179]
	v_pk_mul_f32 v[236:237], v[232:233], v[234:235]
	v_mul_f32_e32 v188, v134, v135
	v_mul_f32_e32 v190, v146, v147
	v_mul_f32_e32 v189, v180, v181
	v_mul_f32_e32 v191, v236, v237
	v_pk_mul_f32 v[192:193], v[188:189], v[190:191]
	v_mul_f32_e32 v174, v192, v193
	v_rcp_f32_e32 v173, v174
	v_pk_add_f32 v[164:165], v[164:165], v[86:87]
	v_pk_add_f32 v[164:165], v[164:165], v[88:89]
	v_pk_add_f32 v[164:165], v[164:165], v[38:39]
	v_pk_add_f32 v[164:165], v[164:165], v[40:41]
	v_pk_add_f32 v[164:165], v[164:165], v[122:123]
	v_pk_add_f32 v[164:165], v[164:165], v[124:125]
	v_pk_add_f32 v[164:165], v[164:165], v[50:51]
	v_pk_add_f32 v[164:165], v[164:165], v[52:53]
	v_pk_mul_f32 v[230:231], v[172:173], v[192:193] op_sel:[1,1] op_sel_hi:[1,0]
	v_pk_mul_f32 v[192:193], v[230:231], v[190:191]
	v_pk_mul_f32 v[190:191], v[230:231], v[188:189]
	v_pk_mul_f32 v[136:137], v[192:193], v[134:135] op_sel:[0,1] op_sel_hi:[0,0]
	v_pk_mul_f32 v[148:149], v[190:191], v[146:147] op_sel:[0,1] op_sel_hi:[0,0]
	v_pk_mul_f32 v[182:183], v[192:193], v[180:181] op_sel:[1,1] op_sel_hi:[1,0]
	v_pk_mul_f32 v[238:239], v[190:191], v[236:237] op_sel:[1,1] op_sel_hi:[1,0]
	v_pk_fma_f32 v[138:139], v[136:137], v[132:133], 1.0 op_sel_hi:[1,1,0]
	v_pk_fma_f32 v[140:141], v[136:137], v[130:131], 1.0 op_sel_hi:[1,1,0]
	v_pk_fma_f32 v[150:151], v[148:149], v[144:145], 1.0 op_sel_hi:[1,1,0]
	v_pk_fma_f32 v[152:153], v[148:149], v[142:143], 1.0 op_sel_hi:[1,1,0]
	v_pk_fma_f32 v[184:185], v[182:183], v[178:179], 1.0 op_sel_hi:[1,1,0]
	v_pk_fma_f32 v[186:187], v[182:183], v[176:177], 1.0 op_sel_hi:[1,1,0]
	v_pk_fma_f32 v[240:241], v[238:239], v[234:235], 1.0 op_sel_hi:[1,1,0]
	v_pk_fma_f32 v[242:243], v[238:239], v[232:233], 1.0 op_sel_hi:[1,1,0]
	v_cvt_pk_bf16_f32 v154, v138, v139
	v_cvt_pk_bf16_f32 v155, v140, v141
	v_cvt_pk_bf16_f32 v156, v150, v151
	v_cvt_pk_bf16_f32 v157, v152, v153
	v_cvt_pk_bf16_f32 v158, v184, v185
	v_cvt_pk_bf16_f32 v159, v186, v187
	v_cvt_pk_bf16_f32 v160, v240, v241
	v_cvt_pk_bf16_f32 v161, v242, v243
	ds_read_b128 v[86:89], v172 offset:512
	ds_read_b128 v[38:41], v172 offset:576
	ds_read_b128 v[122:125], v172 offset:640
	ds_read_b128 v[50:53], v172 offset:704
	v_permlane16_swap_b32_e32 v154, v156
	v_permlane16_swap_b32_e32 v155, v157
	global_store_dwordx4 v228, v[154:157], s[62:63] offset:2048 nt
	v_permlane16_swap_b32_e32 v158, v160
	v_permlane16_swap_b32_e32 v159, v161
	global_store_dwordx4 v228, v[158:161], s[62:63] offset:2176 nt
	v_log_f32_e32 v166, v162
	v_log_f32_e32 v170, v174
	v_add_f32_e32 v168, v164, v165
	v_mul_f32_e32 v168, 0xbeb17218, v168
	v_add_f32_e32 v166, v166, v170
	v_fmac_f32_e32 v168, 0x3f317218, v166
	v_mov_b32_e32 v169, v168
	s_nop 1
	v_permlane16_swap_b32_e32 v168, v169
	v_add_f32_e32 v168, v168, v169
	v_mov_b32_e32 v169, v168
	s_nop 1
	v_permlane32_swap_b32_e32 v168, v169
	v_add_f32_e32 v168, v168, v169
	s_mov_b64 exec, s[0:1]
	global_store_dword v229, v168, s[66:67] offset:64
	s_mov_b64 exec, -1
	v_exp_f32_e32 v130, v98
	v_exp_f32_e32 v131, v99
	v_exp_f32_e32 v132, v100
	v_exp_f32_e32 v133, v101
	v_exp_f32_e32 v142, v62
	v_exp_f32_e32 v143, v63
	v_exp_f32_e32 v144, v64
	v_exp_f32_e32 v145, v65
	v_exp_f32_e32 v176, v94
	v_exp_f32_e32 v177, v95
	v_exp_f32_e32 v178, v96
	v_exp_f32_e32 v179, v97
	v_exp_f32_e32 v232, v54
	v_exp_f32_e32 v233, v55
	v_exp_f32_e32 v234, v56
	v_exp_f32_e32 v235, v57
	v_pk_fma_f32 v[130:131], v[130:131], -0.5, -0.5 op_sel_hi:[1,0,0]
	v_pk_fma_f32 v[132:133], v[132:133], -0.5, -0.5 op_sel_hi:[1,0,0]
	v_pk_fma_f32 v[142:143], v[142:143], -0.5, -0.5 op_sel_hi:[1,0,0]
	v_pk_fma_f32 v[144:145], v[144:145], -0.5, -0.5 op_sel_hi:[1,0,0]
	v_pk_fma_f32 v[176:177], v[176:177], -0.5, -0.5 op_sel_hi:[1,0,0]
	v_pk_fma_f32 v[178:179], v[178:179], -0.5, -0.5 op_sel_hi:[1,0,0]
	v_pk_fma_f32 v[232:233], v[232:233], -0.5, -0.5 op_sel_hi:[1,0,0]
	v_pk_fma_f32 v[234:235], v[234:235], -0.5, -0.5 op_sel_hi:[1,0,0]
	v_pk_mul_f32 v[134:135], v[130:131], v[132:133]
	v_pk_mul_f32 v[146:147], v[142:143], v[144:145]
	v_pk_mul_f32 v[180:181], v[176:177], v[178:179]
	v_pk_mul_f32 v[236:237], v[232:233], v[234:235]
	v_mul_f32_e32 v188, v134, v135
	v_mul_f32_e32 v190, v146, v147
	v_mul_f32_e32 v189, v180, v181
	v_mul_f32_e32 v191, v236, v237
	v_pk_mul_f32 v[192:193], v[188:189], v[190:191]
	v_mul_f32_e32 v162, v192, v193
	v_rcp_f32_e32 v173, v162
	v_pk_add_f32 v[164:165], v[98:99], v[100:101]
	v_pk_add_f32 v[164:165], v[164:165], v[62:63]
	v_pk_add_f32 v[164:165], v[164:165], v[64:65]
	v_pk_add_f32 v[164:165], v[164:165], v[94:95]
	v_pk_add_f32 v[164:165], v[164:165], v[96:97]
	v_pk_add_f32 v[164:165], v[164:165], v[54:55]
	v_pk_add_f32 v[164:165], v[164:165], v[56:57]
	v_pk_mul_f32 v[230:231], v[172:173], v[192:193] op_sel:[1,1] op_sel_hi:[1,0]
	v_pk_mul_f32 v[192:193], v[230:231], v[190:191]
	v_pk_mul_f32 v[190:191], v[230:231], v[188:189]
	v_pk_mul_f32 v[136:137], v[192:193], v[134:135] op_sel:[0,1] op_sel_hi:[0,0]
	v_pk_mul_f32 v[148:149], v[190:191], v[146:147] op_sel:[0,1] op_sel_hi:[0,0]
	v_pk_mul_f32 v[182:183], v[192:193], v[180:181] op_sel:[1,1] op_sel_hi:[1,0]
	v_pk_mul_f32 v[238:239], v[190:191], v[236:237] op_sel:[1,1] op_sel_hi:[1,0]
	v_pk_fma_f32 v[138:139], v[136:137], v[132:133], 1.0 op_sel_hi:[1,1,0]
	v_pk_fma_f32 v[140:141], v[136:137], v[130:131], 1.0 op_sel_hi:[1,1,0]
	v_pk_fma_f32 v[150:151], v[148:149], v[144:145], 1.0 op_sel_hi:[1,1,0]
	v_pk_fma_f32 v[152:153], v[148:149], v[142:143], 1.0 op_sel_hi:[1,1,0]
	v_pk_fma_f32 v[184:185], v[182:183], v[178:179], 1.0 op_sel_hi:[1,1,0]
	v_pk_fma_f32 v[186:187], v[182:183], v[176:177], 1.0 op_sel_hi:[1,1,0]
	v_pk_fma_f32 v[240:241], v[238:239], v[234:235], 1.0 op_sel_hi:[1,1,0]
	v_pk_fma_f32 v[242:243], v[238:239], v[232:233], 1.0 op_sel_hi:[1,1,0]
	v_cvt_pk_bf16_f32 v154, v138, v139
	v_cvt_pk_bf16_f32 v155, v140, v141
	v_cvt_pk_bf16_f32 v156, v150, v151
	v_cvt_pk_bf16_f32 v157, v152, v153
	v_cvt_pk_bf16_f32 v158, v184, v185
	v_cvt_pk_bf16_f32 v159, v186, v187
	v_cvt_pk_bf16_f32 v160, v240, v241
	v_cvt_pk_bf16_f32 v161, v242, v243
	ds_read_b128 v[98:101], v172
	ds_read_b128 v[62:65], v172 offset:64
	ds_read_b128 v[94:97], v172 offset:128
	ds_read_b128 v[54:57], v172 offset:192
	v_permlane16_swap_b32_e32 v154, v156
	v_permlane16_swap_b32_e32 v155, v157
	global_store_dwordx4 v228, v[154:157], s[60:61] nt
	v_permlane16_swap_b32_e32 v158, v160
	v_permlane16_swap_b32_e32 v159, v161
	global_store_dwordx4 v228, v[158:161], s[60:61] offset:128 nt
	v_exp_f32_e32 v130, v82
	v_exp_f32_e32 v131, v83
	v_exp_f32_e32 v132, v84
	v_exp_f32_e32 v133, v85
	v_exp_f32_e32 v142, v34
	v_exp_f32_e32 v143, v35
	v_exp_f32_e32 v144, v36
	v_exp_f32_e32 v145, v37
	v_exp_f32_e32 v176, v118
	v_exp_f32_e32 v177, v119
	v_exp_f32_e32 v178, v120
	v_exp_f32_e32 v179, v121
	v_exp_f32_e32 v232, v46
	v_exp_f32_e32 v233, v47
	v_exp_f32_e32 v234, v48
	v_exp_f32_e32 v235, v49
	v_pk_fma_f32 v[130:131], v[130:131], -0.5, -0.5 op_sel_hi:[1,0,0]
	v_pk_fma_f32 v[132:133], v[132:133], -0.5, -0.5 op_sel_hi:[1,0,0]
	v_pk_fma_f32 v[142:143], v[142:143], -0.5, -0.5 op_sel_hi:[1,0,0]
	v_pk_fma_f32 v[144:145], v[144:145], -0.5, -0.5 op_sel_hi:[1,0,0]
	v_pk_fma_f32 v[176:177], v[176:177], -0.5, -0.5 op_sel_hi:[1,0,0]
	v_pk_fma_f32 v[178:179], v[178:179], -0.5, -0.5 op_sel_hi:[1,0,0]
	v_pk_fma_f32 v[232:233], v[232:233], -0.5, -0.5 op_sel_hi:[1,0,0]
	v_pk_fma_f32 v[234:235], v[234:235], -0.5, -0.5 op_sel_hi:[1,0,0]
	v_pk_mul_f32 v[134:135], v[130:131], v[132:133]
	v_pk_mul_f32 v[146:147], v[142:143], v[144:145]
	v_pk_mul_f32 v[180:181], v[176:177], v[178:179]
	v_pk_mul_f32 v[236:237], v[232:233], v[234:235]
	v_mul_f32_e32 v188, v134, v135
	v_mul_f32_e32 v190, v146, v147
	v_mul_f32_e32 v189, v180, v181
	v_mul_f32_e32 v191, v236, v237
	v_pk_mul_f32 v[192:193], v[188:189], v[190:191]
	v_mul_f32_e32 v174, v192, v193
	v_rcp_f32_e32 v173, v174
	v_pk_add_f32 v[164:165], v[164:165], v[82:83]
	v_pk_add_f32 v[164:165], v[164:165], v[84:85]
	v_pk_add_f32 v[164:165], v[164:165], v[34:35]
	v_pk_add_f32 v[164:165], v[164:165], v[36:37]
	v_pk_add_f32 v[164:165], v[164:165], v[118:119]
	v_pk_add_f32 v[164:165], v[164:165], v[120:121]
	v_pk_add_f32 v[164:165], v[164:165], v[46:47]
	v_pk_add_f32 v[164:165], v[164:165], v[48:49]
	v_pk_mul_f32 v[230:231], v[172:173], v[192:193] op_sel:[1,1] op_sel_hi:[1,0]
	v_pk_mul_f32 v[192:193], v[230:231], v[190:191]
	v_pk_mul_f32 v[190:191], v[230:231], v[188:189]
	v_pk_mul_f32 v[136:137], v[192:193], v[134:135] op_sel:[0,1] op_sel_hi:[0,0]
	v_pk_mul_f32 v[148:149], v[190:191], v[146:147] op_sel:[0,1] op_sel_hi:[0,0]
	v_pk_mul_f32 v[182:183], v[192:193], v[180:181] op_sel:[1,1] op_sel_hi:[1,0]
	v_pk_mul_f32 v[238:239], v[190:191], v[236:237] op_sel:[1,1] op_sel_hi:[1,0]
	v_pk_fma_f32 v[138:139], v[136:137], v[132:133], 1.0 op_sel_hi:[1,1,0]
	v_pk_fma_f32 v[140:141], v[136:137], v[130:131], 1.0 op_sel_hi:[1,1,0]
	v_pk_fma_f32 v[150:151], v[148:149], v[144:145], 1.0 op_sel_hi:[1,1,0]
	v_pk_fma_f32 v[152:153], v[148:149], v[142:143], 1.0 op_sel_hi:[1,1,0]
	v_pk_fma_f32 v[184:185], v[182:183], v[178:179], 1.0 op_sel_hi:[1,1,0]
	v_pk_fma_f32 v[186:187], v[182:183], v[176:177], 1.0 op_sel_hi:[1,1,0]
	v_pk_fma_f32 v[240:241], v[238:239], v[234:235], 1.0 op_sel_hi:[1,1,0]
	v_pk_fma_f32 v[242:243], v[238:239], v[232:233], 1.0 op_sel_hi:[1,1,0]
	v_cvt_pk_bf16_f32 v154, v138, v139
	v_cvt_pk_bf16_f32 v155, v140, v141
	v_cvt_pk_bf16_f32 v156, v150, v151
	v_cvt_pk_bf16_f32 v157, v152, v153
	v_cvt_pk_bf16_f32 v158, v184, v185
	v_cvt_pk_bf16_f32 v159, v186, v187
	v_cvt_pk_bf16_f32 v160, v240, v241
	v_cvt_pk_bf16_f32 v161, v242, v243
	ds_read_b128 v[82:85], v172 offset:512
	ds_read_b128 v[34:37], v172 offset:576
	ds_read_b128 v[118:121], v172 offset:640
	ds_read_b128 v[46:49], v172 offset:704
	v_permlane16_swap_b32_e32 v154, v156
	v_permlane16_swap_b32_e32 v155, v157
	global_store_dwordx4 v228, v[154:157], s[64:65] nt
	v_permlane16_swap_b32_e32 v158, v160
	v_permlane16_swap_b32_e32 v159, v161
	global_store_dwordx4 v228, v[158:161], s[64:65] offset:128 nt
	v_log_f32_e32 v166, v162
	v_log_f32_e32 v170, v174
	v_add_f32_e32 v168, v164, v165
	v_mul_f32_e32 v168, 0xbeb17218, v168
	v_add_f32_e32 v166, v166, v170
	v_fmac_f32_e32 v168, 0x3f317218, v166
	v_mov_b32_e32 v169, v168
	s_nop 1
	v_permlane16_swap_b32_e32 v168, v169
	v_add_f32_e32 v168, v168, v169
	v_mov_b32_e32 v169, v168
	s_nop 1
	v_permlane32_swap_b32_e32 v168, v169
	v_add_f32_e32 v168, v168, v169
	s_mov_b64 exec, s[0:1]
	global_store_dword v229, v168, s[66:67] offset:512
	s_mov_b64 exec, -1
	v_exp_f32_e32 v130, v18
	v_exp_f32_e32 v131, v19
	v_exp_f32_e32 v132, v20
	v_exp_f32_e32 v133, v21
	v_exp_f32_e32 v142, v2
	v_exp_f32_e32 v143, v3
	v_exp_f32_e32 v144, v4
	v_exp_f32_e32 v145, v5
	v_exp_f32_e32 v176, v26
	v_exp_f32_e32 v177, v27
	v_exp_f32_e32 v178, v28
	v_exp_f32_e32 v179, v29
	v_exp_f32_e32 v232, v10
	v_exp_f32_e32 v233, v11
	v_exp_f32_e32 v234, v12
	v_exp_f32_e32 v235, v13
	v_pk_fma_f32 v[130:131], v[130:131], -0.5, -0.5 op_sel_hi:[1,0,0]
	v_pk_fma_f32 v[132:133], v[132:133], -0.5, -0.5 op_sel_hi:[1,0,0]
	v_pk_fma_f32 v[142:143], v[142:143], -0.5, -0.5 op_sel_hi:[1,0,0]
	v_pk_fma_f32 v[144:145], v[144:145], -0.5, -0.5 op_sel_hi:[1,0,0]
	v_pk_fma_f32 v[176:177], v[176:177], -0.5, -0.5 op_sel_hi:[1,0,0]
	v_pk_fma_f32 v[178:179], v[178:179], -0.5, -0.5 op_sel_hi:[1,0,0]
	v_pk_fma_f32 v[232:233], v[232:233], -0.5, -0.5 op_sel_hi:[1,0,0]
	v_pk_fma_f32 v[234:235], v[234:235], -0.5, -0.5 op_sel_hi:[1,0,0]
	v_pk_mul_f32 v[134:135], v[130:131], v[132:133]
	v_pk_mul_f32 v[146:147], v[142:143], v[144:145]
	v_pk_mul_f32 v[180:181], v[176:177], v[178:179]
	v_pk_mul_f32 v[236:237], v[232:233], v[234:235]
	v_mul_f32_e32 v188, v134, v135
	v_mul_f32_e32 v190, v146, v147
	v_mul_f32_e32 v189, v180, v181
	v_mul_f32_e32 v191, v236, v237
	v_pk_mul_f32 v[192:193], v[188:189], v[190:191]
	v_mul_f32_e32 v162, v192, v193
	v_rcp_f32_e32 v173, v162
	v_pk_add_f32 v[164:165], v[18:19], v[20:21]
	v_pk_add_f32 v[164:165], v[164:165], v[2:3]
	v_pk_add_f32 v[164:165], v[164:165], v[4:5]
	v_pk_add_f32 v[164:165], v[164:165], v[26:27]
	v_pk_add_f32 v[164:165], v[164:165], v[28:29]
	v_pk_add_f32 v[164:165], v[164:165], v[10:11]
	v_pk_add_f32 v[164:165], v[164:165], v[12:13]
	v_pk_mul_f32 v[230:231], v[172:173], v[192:193] op_sel:[1,1] op_sel_hi:[1,0]
	v_pk_mul_f32 v[192:193], v[230:231], v[190:191]
	v_pk_mul_f32 v[190:191], v[230:231], v[188:189]
	v_pk_mul_f32 v[136:137], v[192:193], v[134:135] op_sel:[0,1] op_sel_hi:[0,0]
	v_pk_mul_f32 v[148:149], v[190:191], v[146:147] op_sel:[0,1] op_sel_hi:[0,0]
	v_pk_mul_f32 v[182:183], v[192:193], v[180:181] op_sel:[1,1] op_sel_hi:[1,0]
	v_pk_mul_f32 v[238:239], v[190:191], v[236:237] op_sel:[1,1] op_sel_hi:[1,0]
	v_pk_fma_f32 v[138:139], v[136:137], v[132:133], 1.0 op_sel_hi:[1,1,0]
	v_pk_fma_f32 v[140:141], v[136:137], v[130:131], 1.0 op_sel_hi:[1,1,0]
	v_pk_fma_f32 v[150:151], v[148:149], v[144:145], 1.0 op_sel_hi:[1,1,0]
	v_pk_fma_f32 v[152:153], v[148:149], v[142:143], 1.0 op_sel_hi:[1,1,0]
	v_pk_fma_f32 v[184:185], v[182:183], v[178:179], 1.0 op_sel_hi:[1,1,0]
	v_pk_fma_f32 v[186:187], v[182:183], v[176:177], 1.0 op_sel_hi:[1,1,0]
	v_pk_fma_f32 v[240:241], v[238:239], v[234:235], 1.0 op_sel_hi:[1,1,0]
	v_pk_fma_f32 v[242:243], v[238:239], v[232:233], 1.0 op_sel_hi:[1,1,0]
	v_cvt_pk_bf16_f32 v154, v138, v139
	v_cvt_pk_bf16_f32 v155, v140, v141
	v_cvt_pk_bf16_f32 v156, v150, v151
	v_cvt_pk_bf16_f32 v157, v152, v153
	v_cvt_pk_bf16_f32 v158, v184, v185
	v_cvt_pk_bf16_f32 v159, v186, v187
	v_cvt_pk_bf16_f32 v160, v240, v241
	v_cvt_pk_bf16_f32 v161, v242, v243
	ds_read_b128 v[18:21], v172
	ds_read_b128 v[2:5], v172 offset:64
	ds_read_b128 v[26:29], v172 offset:128
	ds_read_b128 v[10:13], v172 offset:192
	v_permlane16_swap_b32_e32 v154, v156
	v_permlane16_swap_b32_e32 v155, v157
	global_store_dwordx4 v228, v[154:157], s[60:61] offset:2048 nt
	v_permlane16_swap_b32_e32 v158, v160
	v_permlane16_swap_b32_e32 v159, v161
	global_store_dwordx4 v228, v[158:161], s[60:61] offset:2176 nt
	v_exp_f32_e32 v130, v22
	v_exp_f32_e32 v131, v23
	v_exp_f32_e32 v132, v24
	v_exp_f32_e32 v133, v25
	v_exp_f32_e32 v142, v6
	v_exp_f32_e32 v143, v7
	v_exp_f32_e32 v144, v8
	v_exp_f32_e32 v145, v9
	v_exp_f32_e32 v176, v30
	v_exp_f32_e32 v177, v31
	v_exp_f32_e32 v178, v32
	v_exp_f32_e32 v179, v33
	v_exp_f32_e32 v232, v14
	v_exp_f32_e32 v233, v15
	v_exp_f32_e32 v234, v16
	v_exp_f32_e32 v235, v17
	v_pk_fma_f32 v[130:131], v[130:131], -0.5, -0.5 op_sel_hi:[1,0,0]
	v_pk_fma_f32 v[132:133], v[132:133], -0.5, -0.5 op_sel_hi:[1,0,0]
	v_pk_fma_f32 v[142:143], v[142:143], -0.5, -0.5 op_sel_hi:[1,0,0]
	v_pk_fma_f32 v[144:145], v[144:145], -0.5, -0.5 op_sel_hi:[1,0,0]
	v_pk_fma_f32 v[176:177], v[176:177], -0.5, -0.5 op_sel_hi:[1,0,0]
	v_pk_fma_f32 v[178:179], v[178:179], -0.5, -0.5 op_sel_hi:[1,0,0]
	v_pk_fma_f32 v[232:233], v[232:233], -0.5, -0.5 op_sel_hi:[1,0,0]
	v_pk_fma_f32 v[234:235], v[234:235], -0.5, -0.5 op_sel_hi:[1,0,0]
	v_pk_mul_f32 v[134:135], v[130:131], v[132:133]
	v_pk_mul_f32 v[146:147], v[142:143], v[144:145]
	v_pk_mul_f32 v[180:181], v[176:177], v[178:179]
	v_pk_mul_f32 v[236:237], v[232:233], v[234:235]
	v_mul_f32_e32 v188, v134, v135
	v_mul_f32_e32 v190, v146, v147
	v_mul_f32_e32 v189, v180, v181
	v_mul_f32_e32 v191, v236, v237
	v_pk_mul_f32 v[192:193], v[188:189], v[190:191]
	v_mul_f32_e32 v174, v192, v193
	v_rcp_f32_e32 v173, v174
	v_pk_add_f32 v[164:165], v[164:165], v[22:23]
	v_pk_add_f32 v[164:165], v[164:165], v[24:25]
	v_pk_add_f32 v[164:165], v[164:165], v[6:7]
	v_pk_add_f32 v[164:165], v[164:165], v[8:9]
	v_pk_add_f32 v[164:165], v[164:165], v[30:31]
	v_pk_add_f32 v[164:165], v[164:165], v[32:33]
	v_pk_add_f32 v[164:165], v[164:165], v[14:15]
	v_pk_add_f32 v[164:165], v[164:165], v[16:17]
	v_pk_mul_f32 v[230:231], v[172:173], v[192:193] op_sel:[1,1] op_sel_hi:[1,0]
	v_pk_mul_f32 v[192:193], v[230:231], v[190:191]
	v_pk_mul_f32 v[190:191], v[230:231], v[188:189]
	v_pk_mul_f32 v[136:137], v[192:193], v[134:135] op_sel:[0,1] op_sel_hi:[0,0]
	v_pk_mul_f32 v[148:149], v[190:191], v[146:147] op_sel:[0,1] op_sel_hi:[0,0]
	v_pk_mul_f32 v[182:183], v[192:193], v[180:181] op_sel:[1,1] op_sel_hi:[1,0]
	v_pk_mul_f32 v[238:239], v[190:191], v[236:237] op_sel:[1,1] op_sel_hi:[1,0]
	v_pk_fma_f32 v[138:139], v[136:137], v[132:133], 1.0 op_sel_hi:[1,1,0]
	v_pk_fma_f32 v[140:141], v[136:137], v[130:131], 1.0 op_sel_hi:[1,1,0]
	v_pk_fma_f32 v[150:151], v[148:149], v[144:145], 1.0 op_sel_hi:[1,1,0]
	v_pk_fma_f32 v[152:153], v[148:149], v[142:143], 1.0 op_sel_hi:[1,1,0]
	v_pk_fma_f32 v[184:185], v[182:183], v[178:179], 1.0 op_sel_hi:[1,1,0]
	v_pk_fma_f32 v[186:187], v[182:183], v[176:177], 1.0 op_sel_hi:[1,1,0]
	v_pk_fma_f32 v[240:241], v[238:239], v[234:235], 1.0 op_sel_hi:[1,1,0]
	v_pk_fma_f32 v[242:243], v[238:239], v[232:233], 1.0 op_sel_hi:[1,1,0]
	v_cvt_pk_bf16_f32 v154, v138, v139
	v_cvt_pk_bf16_f32 v155, v140, v141
	v_cvt_pk_bf16_f32 v156, v150, v151
	v_cvt_pk_bf16_f32 v157, v152, v153
	v_cvt_pk_bf16_f32 v158, v184, v185
	v_cvt_pk_bf16_f32 v159, v186, v187
	v_cvt_pk_bf16_f32 v160, v240, v241
	v_cvt_pk_bf16_f32 v161, v242, v243
	ds_read_b128 v[22:25], v172 offset:512
	ds_read_b128 v[6:9], v172 offset:576
	ds_read_b128 v[30:33], v172 offset:640
	ds_read_b128 v[14:17], v172 offset:704
	v_permlane16_swap_b32_e32 v154, v156
	v_permlane16_swap_b32_e32 v155, v157
	global_store_dwordx4 v228, v[154:157], s[64:65] offset:2048 nt
	v_permlane16_swap_b32_e32 v158, v160
	v_permlane16_swap_b32_e32 v159, v161
	global_store_dwordx4 v228, v[158:161], s[64:65] offset:2176 nt
	v_log_f32_e32 v166, v162
	v_log_f32_e32 v170, v174
	v_add_f32_e32 v168, v164, v165
	v_mul_f32_e32 v168, 0xbeb17218, v168
	v_add_f32_e32 v166, v166, v170
	v_fmac_f32_e32 v168, 0x3f317218, v166
	v_mov_b32_e32 v169, v168
	s_nop 1
	v_permlane16_swap_b32_e32 v168, v169
	v_add_f32_e32 v168, v168, v169
	v_mov_b32_e32 v169, v168
	s_nop 1
	v_permlane32_swap_b32_e32 v168, v169
	v_add_f32_e32 v168, v168, v169
	s_mov_b64 exec, s[0:1]
	global_store_dword v229, v168, s[66:67] offset:576
	s_mov_b64 exec, -1
	s_cmp_eq_u32 s40, 8
	s_cbranch_scc1 .Lg1_last_tile
	s_mov_b32 s2, s40
	s_add_i32 s40, s40, 1
	s_mov_b32 s41, s12
	s_lshl_b32 s12, s40, 5
	s_cmp_eq_u32 s2, 7
	s_cselect_b64 s[2:3], -1, 0
	s_and_b64 s[16:17], s[2:3], exec
	s_cselect_b32 s12, 0xe0, s12
	s_add_i32 s16, s12, s18
	s_lshr_b32 s12, s16, 4
	s_and_b32 s12, s12, 0xfffff8
	s_lshl_b32 s16, s16, 5
	s_mov_b32 s42, s35
	s_or_b32 s12, s12, s19
	s_and_b32 s35, s16, 0xf00
	s_lshl_b32 s16, s40, 10
	s_lshl_b32 s12, s12, 8
	s_and_b32 s43, s16, 0x400
	s_or_b64 s[2:3], vcc, s[2:3]
	s_lshl_b32 s44, s41, 7
	v_lshl_add_u64 v[202:203], s[12:13], 2, v[196:197]
	s_mov_b32 s45, 0x404000
	s_xor_b64 s[2:3], s[2:3], -1
	v_add_u32_e32 v194, s43, v208
	s_mov_b32 s46, 0
	s_bitcmp1_b32 s20, 12
	s_cbranch_scc0 .Lg1_noY
	s_barrier
.Lg1_noY:
	s_branch .LBB3_7
.Lg1_last_tile:
	s_bitcmp1_b32 s20, 12
	s_cbranch_scc0 .Lg1_noY2
	s_barrier
